# baseline (speedup 1.0000x reference)
.Lpre_not160:
	s_cmpk_lt_u32 s2, 0xad
	s_cbranch_scc1 .Lpre_roleD
	s_branch .Lpre_roleE
.Lpre_roleA_new:
	s_load_dwordx4 s[4:7], s[0:1], 0x0
	s_load_dwordx2 s[8:9], s[0:1], 0x18
	s_load_dwordx2 s[10:11], s[0:1], 0x58
	s_lshr_b32 s3, s2, 3
	s_and_b32 s12, s2, 7
	v_and_b32_e32 v1, 15, v0
	v_lshrrev_b32_e32 v2, 4, v0
	v_lshlrev_b32_e32 v3, 5, v0
	v_lshlrev_b32_e32 v4, 13, v2
	v_lshl_or_b32 v4, v1, 2, v4
	v_add_u32_e32 v5, 0x1000, v4
	v_and_b32_e32 v6, 7, v2
	v_lshlrev_b32_e32 v6, 2, v6
	v_and_b32_e32 v7, 7, v0
	v_lshlrev_b32_e32 v7, 2, v7
	s_lshl_b32 s13, s3, 13
	s_lshl_b32 s14, s12, 6
	s_lshl_b32 s15, s3, 5
	s_waitcnt lgkmcnt(0)
	s_add_u32 s16, s4, s13
	s_addc_u32 s17, s5, 0
	s_add_u32 s18, s6, s14
	s_addc_u32 s19, s7, 0
	s_add_u32 s20, s8, s15
	s_addc_u32 s21, s9, 0
	global_load_dwordx4 v[8:11], v3, s[16:17]
	global_load_dwordx4 v[12:15], v3, s[16:17] offset:16
	global_load_dword v16, v4, s[18:19]
	global_load_dword v17, v4, s[18:19] offset:512
	global_load_dword v18, v4, s[18:19] offset:1024
	global_load_dword v19, v4, s[18:19] offset:1536
	global_load_dword v20, v4, s[18:19] offset:2048
	global_load_dword v21, v4, s[18:19] offset:2560
	global_load_dword v22, v4, s[18:19] offset:3072
	global_load_dword v23, v4, s[18:19] offset:3584
	global_load_dword v24, v5, s[18:19]
	global_load_dword v25, v5, s[18:19] offset:512
	global_load_dword v26, v5, s[18:19] offset:1024
	global_load_dword v27, v5, s[18:19] offset:1536
	global_load_dword v28, v5, s[18:19] offset:2048
	global_load_dword v29, v5, s[18:19] offset:2560
	global_load_dword v30, v5, s[18:19] offset:3072
	global_load_dword v31, v5, s[18:19] offset:3584
	global_load_dword v72, v6, s[20:21]
	global_load_dword v73, v7, s[20:21]
	s_waitcnt vmcnt(18)
	ds_write_b128 v3, v[8:11]
	ds_write_b128 v3, v[12:15] offset:16
	v_lshlrev_b32_e32 v74, 6, v2
	v_lshlrev_b32_e32 v75, 9, v2
	v_lshl_or_b32 v75, v1, 2, v75
	s_waitcnt lgkmcnt(0)
	s_barrier
	ds_read_b128 v[32:35], v74 offset:0
	ds_read_b128 v[36:39], v74 offset:16
	ds_read_b128 v[40:43], v74 offset:32
	ds_read_b128 v[44:47], v74 offset:48
	s_waitcnt vmcnt(2)
	ds_read_b128 v[48:51], v74 offset:1024
	ds_read_b128 v[52:55], v74 offset:1040
	ds_read_b128 v[56:59], v74 offset:1056
	ds_read_b128 v[60:63], v74 offset:1072
	s_waitcnt lgkmcnt(4)
	v_mul_f32_e32 v64, v32, v16
	v_fmac_f32_e32 v64, v33, v17
	v_fmac_f32_e32 v64, v34, v18
	v_fmac_f32_e32 v64, v35, v19
	v_fmac_f32_e32 v64, v36, v20
	v_fmac_f32_e32 v64, v37, v21
	v_fmac_f32_e32 v64, v38, v22
	v_fmac_f32_e32 v64, v39, v23
	v_fmac_f32_e32 v64, v40, v24
	v_fmac_f32_e32 v64, v41, v25
	v_fmac_f32_e32 v64, v42, v26
	v_fmac_f32_e32 v64, v43, v27
	v_fmac_f32_e32 v64, v44, v28
	v_fmac_f32_e32 v64, v45, v29
	v_fmac_f32_e32 v64, v46, v30
	v_fmac_f32_e32 v64, v47, v31
	ds_read_b128 v[32:35], v74 offset:2048
	ds_read_b128 v[36:39], v74 offset:2064
	ds_read_b128 v[40:43], v74 offset:2080
	ds_read_b128 v[44:47], v74 offset:2096
	s_waitcnt lgkmcnt(4)
	v_mul_f32_e32 v65, v48, v16
	v_fmac_f32_e32 v65, v49, v17
	v_fmac_f32_e32 v65, v50, v18
	v_fmac_f32_e32 v65, v51, v19
	v_fmac_f32_e32 v65, v52, v20
	v_fmac_f32_e32 v65, v53, v21
	v_fmac_f32_e32 v65, v54, v22
	v_fmac_f32_e32 v65, v55, v23
	v_fmac_f32_e32 v65, v56, v24
	v_fmac_f32_e32 v65, v57, v25
	v_fmac_f32_e32 v65, v58, v26
	v_fmac_f32_e32 v65, v59, v27
	v_fmac_f32_e32 v65, v60, v28
	v_fmac_f32_e32 v65, v61, v29
	v_fmac_f32_e32 v65, v62, v30
	v_fmac_f32_e32 v65, v63, v31
	ds_read_b128 v[48:51], v74 offset:3072
	ds_read_b128 v[52:55], v74 offset:3088
	ds_read_b128 v[56:59], v74 offset:3104
	ds_read_b128 v[60:63], v74 offset:3120
	s_waitcnt lgkmcnt(4)
	v_mul_f32_e32 v66, v32, v16
	v_fmac_f32_e32 v66, v33, v17
	v_fmac_f32_e32 v66, v34, v18
	v_fmac_f32_e32 v66, v35, v19
	v_fmac_f32_e32 v66, v36, v20
	v_fmac_f32_e32 v66, v37, v21
	v_fmac_f32_e32 v66, v38, v22
	v_fmac_f32_e32 v66, v39, v23
	v_fmac_f32_e32 v66, v40, v24
	v_fmac_f32_e32 v66, v41, v25
	v_fmac_f32_e32 v66, v42, v26
	v_fmac_f32_e32 v66, v43, v27
	v_fmac_f32_e32 v66, v44, v28
	v_fmac_f32_e32 v66, v45, v29
	v_fmac_f32_e32 v66, v46, v30
	v_fmac_f32_e32 v66, v47, v31
	ds_read_b128 v[32:35], v74 offset:4096
	ds_read_b128 v[36:39], v74 offset:4112
	ds_read_b128 v[40:43], v74 offset:4128
	ds_read_b128 v[44:47], v74 offset:4144
	s_waitcnt lgkmcnt(4)
	v_mul_f32_e32 v67, v48, v16
	v_fmac_f32_e32 v67, v49, v17
	v_fmac_f32_e32 v67, v50, v18
	v_fmac_f32_e32 v67, v51, v19
	v_fmac_f32_e32 v67, v52, v20
	v_fmac_f32_e32 v67, v53, v21
	v_fmac_f32_e32 v67, v54, v22
	v_fmac_f32_e32 v67, v55, v23
	v_fmac_f32_e32 v67, v56, v24
	v_fmac_f32_e32 v67, v57, v25
	v_fmac_f32_e32 v67, v58, v26
	v_fmac_f32_e32 v67, v59, v27
	v_fmac_f32_e32 v67, v60, v28
	v_fmac_f32_e32 v67, v61, v29
	v_fmac_f32_e32 v67, v62, v30
	v_fmac_f32_e32 v67, v63, v31
	ds_read_b128 v[48:51], v74 offset:5120
	ds_read_b128 v[52:55], v74 offset:5136
	ds_read_b128 v[56:59], v74 offset:5152
	ds_read_b128 v[60:63], v74 offset:5168
	s_waitcnt lgkmcnt(4)
	v_mul_f32_e32 v68, v32, v16
	v_fmac_f32_e32 v68, v33, v17
	v_fmac_f32_e32 v68, v34, v18
	v_fmac_f32_e32 v68, v35, v19
	v_fmac_f32_e32 v68, v36, v20
	v_fmac_f32_e32 v68, v37, v21
	v_fmac_f32_e32 v68, v38, v22
	v_fmac_f32_e32 v68, v39, v23
	v_fmac_f32_e32 v68, v40, v24
	v_fmac_f32_e32 v68, v41, v25
	v_fmac_f32_e32 v68, v42, v26
	v_fmac_f32_e32 v68, v43, v27
	v_fmac_f32_e32 v68, v44, v28
	v_fmac_f32_e32 v68, v45, v29
	v_fmac_f32_e32 v68, v46, v30
	v_fmac_f32_e32 v68, v47, v31
	ds_read_b128 v[32:35], v74 offset:6144
	ds_read_b128 v[36:39], v74 offset:6160
	ds_read_b128 v[40:43], v74 offset:6176
	ds_read_b128 v[44:47], v74 offset:6192
	s_waitcnt lgkmcnt(4)
	v_mul_f32_e32 v69, v48, v16
	v_fmac_f32_e32 v69, v49, v17
	v_fmac_f32_e32 v69, v50, v18
	v_fmac_f32_e32 v69, v51, v19
	v_fmac_f32_e32 v69, v52, v20
	v_fmac_f32_e32 v69, v53, v21
	v_fmac_f32_e32 v69, v54, v22
	v_fmac_f32_e32 v69, v55, v23
	v_fmac_f32_e32 v69, v56, v24
	v_fmac_f32_e32 v69, v57, v25
	v_fmac_f32_e32 v69, v58, v26
	v_fmac_f32_e32 v69, v59, v27
	v_fmac_f32_e32 v69, v60, v28
	v_fmac_f32_e32 v69, v61, v29
	v_fmac_f32_e32 v69, v62, v30
	v_fmac_f32_e32 v69, v63, v31
	ds_read_b128 v[48:51], v74 offset:7168
	ds_read_b128 v[52:55], v74 offset:7184
	ds_read_b128 v[56:59], v74 offset:7200
	ds_read_b128 v[60:63], v74 offset:7216
	s_waitcnt lgkmcnt(4)
	v_mul_f32_e32 v70, v32, v16
	v_fmac_f32_e32 v70, v33, v17
	v_fmac_f32_e32 v70, v34, v18
	v_fmac_f32_e32 v70, v35, v19
	v_fmac_f32_e32 v70, v36, v20
	v_fmac_f32_e32 v70, v37, v21
	v_fmac_f32_e32 v70, v38, v22
	v_fmac_f32_e32 v70, v39, v23
	v_fmac_f32_e32 v70, v40, v24
	v_fmac_f32_e32 v70, v41, v25
	v_fmac_f32_e32 v70, v42, v26
	v_fmac_f32_e32 v70, v43, v27
	v_fmac_f32_e32 v70, v44, v28
	v_fmac_f32_e32 v70, v45, v29
	v_fmac_f32_e32 v70, v46, v30
	v_fmac_f32_e32 v70, v47, v31
	s_waitcnt lgkmcnt(0)
	v_mul_f32_e32 v71, v48, v16
	v_fmac_f32_e32 v71, v49, v17
	v_fmac_f32_e32 v71, v50, v18
	v_fmac_f32_e32 v71, v51, v19
	v_fmac_f32_e32 v71, v52, v20
	v_fmac_f32_e32 v71, v53, v21
	v_fmac_f32_e32 v71, v54, v22
	v_fmac_f32_e32 v71, v55, v23
	v_fmac_f32_e32 v71, v56, v24
	v_fmac_f32_e32 v71, v57, v25
	v_fmac_f32_e32 v71, v58, v26
	v_fmac_f32_e32 v71, v59, v27
	v_fmac_f32_e32 v71, v60, v28
	v_fmac_f32_e32 v71, v61, v29
	v_fmac_f32_e32 v71, v62, v30
	v_fmac_f32_e32 v71, v63, v31
	ds_write_b32 v75, v64 offset:8192
	ds_write_b32 v75, v65 offset:8256
	ds_write_b32 v75, v66 offset:8320
	ds_write_b32 v75, v67 offset:8384
	ds_write_b32 v75, v68 offset:8448
	ds_write_b32 v75, v69 offset:8512
	ds_write_b32 v75, v70 offset:8576
	ds_write_b32 v75, v71 offset:8640
	s_lshr_b32 s22, s3, 1
	s_lshr_b32 s23, s22, 2
	s_mul_i32 s23, s23, 20
	s_and_b32 s24, s22, 3
	s_mul_i32 s24, s24, 5
	s_add_u32 s23, s23, s24
	s_and_b32 s25, s3, 1
	s_lshl_b32 s25, s25, 9
	s_lshr_b32 s26, s12, 1
	s_add_u32 s26, s26, s23
	s_lshl_b32 s26, s26, 10
	s_and_b32 s27, s12, 1
	s_lshl_b32 s27, s27, 8
	s_add_u32 s26, s26, s25
	s_add_u32 s26, s26, s27
	s_add_u32 s28, s10, s26
	s_addc_u32 s29, s11, 0
	s_add_u32 s30, s23, 4
	s_lshl_b32 s30, s30, 10
	s_add_u32 s30, s30, s25
	s_add_u32 s30, s10, s30
	s_addc_u32 s31, s11, 0
	s_waitcnt lgkmcnt(0)
	s_barrier
	v_cmp_gt_u32_e32 vcc, 0x80, v0
	s_and_saveexec_b64 s[32:33], vcc
	s_cbranch_execz .Lpre_A_main_done
	v_lshlrev_b32_e32 v76, 2, v0
	ds_read_b32 v32, v76 offset:8192
	ds_read_b32 v33, v76 offset:8704
	ds_read_b32 v34, v76 offset:9216
	ds_read_b32 v35, v76 offset:9728
	ds_read_b32 v36, v76 offset:10240
	ds_read_b32 v37, v76 offset:10752
	ds_read_b32 v38, v76 offset:11264
	ds_read_b32 v39, v76 offset:11776
	s_waitcnt lgkmcnt(0)
	ds_read_b32 v40, v76 offset:12288
	ds_read_b32 v41, v76 offset:12800
	ds_read_b32 v42, v76 offset:13312
	ds_read_b32 v43, v76 offset:13824
	ds_read_b32 v44, v76 offset:14336
	ds_read_b32 v45, v76 offset:14848
	ds_read_b32 v46, v76 offset:15360
	ds_read_b32 v47, v76 offset:15872
	s_waitcnt lgkmcnt(0)
	v_add_f32_e32 v32, v32, v33
	v_add_f32_e32 v32, v32, v34
	v_add_f32_e32 v32, v32, v35
	v_add_f32_e32 v32, v32, v36
	v_add_f32_e32 v32, v32, v37
	v_add_f32_e32 v32, v32, v38
	v_add_f32_e32 v32, v32, v39
	v_add_f32_e32 v32, v32, v40
	v_add_f32_e32 v32, v32, v41
	v_add_f32_e32 v32, v32, v42
	v_add_f32_e32 v32, v32, v43
	v_add_f32_e32 v32, v32, v44
	v_add_f32_e32 v32, v32, v45
	v_add_f32_e32 v32, v32, v46
	v_add_f32_e32 v32, v32, v47
	s_waitcnt vmcnt(0)
	v_mul_f32_e32 v32, v72, v32
	v_cvt_pk_bf16_f32 v32, v32, v32
	v_lshlrev_b32_e32 v77, 4, v1
	v_lshl_or_b32 v77, v2, 1, v77
	global_store_short v77, v32, s[28:29]

.Lpre_E_exit:
	s_endpgm
.Lpre_roleBC:
	s_load_dwordx16 s[4:19], s[0:1], 0x0
	s_load_dwordx8 s[20:27], s[0:1], 0x40
	s_load_dwordx2 s[28:29], s[0:1], 0x60
	s_load_dwordx2 s[30:31], s[0:1], 0xa0
	s_sub_u32 s3, s2, 0x80
	v_lshrrev_b32_e32 v1, 6, v0
	v_and_b32_e32 v2, 63, v0
	v_and_b32_e32 v3, 31, v0
	v_bfe_u32 v4, v0, 5, 1
	v_lshlrev_b32_e32 v30, 4, v0
	v_lshlrev_b32_e32 v5, 7, v1
	v_lshl_or_b32 v5, v3, 2, v5
	s_waitcnt lgkmcnt(0)
	s_lshl_b32 s44, s3, 12
	s_add_u32 s44, s44, 0xa000
	s_add_u32 s26, s26, s44
	s_addc_u32 s27, s27, 0
	s_cmp_lt_u32 s3, 8
	s_cbranch_scc0 .Lpre_B_only
	v_lshrrev_b32_e32 v6, 3, v0
	v_and_b32_e32 v7, 7, v0
	v_lshlrev_b32_e32 v8, 12, v6
	v_lshl_or_b32 v8, v7, 4, v8
	v_lshlrev_b32_e32 v9, 4, v6
	v_lshrrev_b32_e32 v10, 5, v0
	v_lshlrev_b32_e32 v11, 11, v10
	v_lshl_or_b32 v11, v3, 4, v11
	v_lshlrev_b32_e32 v12, 10, v10
	v_lshl_or_b32 v12, v3, 4, v12
	v_lshlrev_b32_e32 v13, 3, v10
	v_and_b32_e32 v14, 0x7f, v0
	v_lshlrev_b32_e32 v14, 2, v14
	s_lshl_b32 s45, s3, 7
	s_add_u32 s36, s4, s45
	s_addc_u32 s37, s5, 0
	s_lshl_b32 s45, s3, 14
	s_add_u32 s38, s6, s45
	s_addc_u32 s39, s7, 0
	s_lshl_b32 s45, s3, 13
	s_add_u32 s40, s18, s45
	s_addc_u32 s41, s19, 0
	s_add_u32 s32, s6, s45
	s_addc_u32 s33, s7, 0
	s_lshl_b32 s45, s3, 6
	s_add_u32 s42, s16, s45
	s_addc_u32 s43, s17, 0
	v_lshl_add_u32 v15, v4, 12, v5
	global_load_dwordx4 v[32:35], v8, s[36:37]
	global_load_dwordx4 v[36:39], v8, s[36:37] offset:1024
	global_load_dwordx4 v[40:43], v8, s[36:37] offset:2048
	global_load_dwordx4 v[44:47], v8, s[36:37] offset:3072
	global_load_dwordx4 v[48:51], v9, s[12:13]
	global_load_dwordx4 v[52:55], v11, s[38:39]
	global_load_dwordx4 v[56:59], v11, s[38:39] offset:512
	global_load_dwordx4 v[60:63], v11, s[38:39] offset:1024
	global_load_dwordx4 v[64:67], v11, s[38:39] offset:1536
	global_load_dwordx4 v[68:71], v12, s[40:41]
	global_load_dwordx4 v[72:75], v12, s[40:41] offset:512
	global_load_dwordx2 v[76:77], v13, s[42:43]
	global_load_dword v78, v14, s[8:9]
	global_load_dword v79, v14, s[20:21]
	global_load_dword v80, v14, s[24:25]
	global_load_dword v16, v15, s[32:33]
	global_load_dword v17, v15, s[32:33] offset:512
	global_load_dword v18, v15, s[32:33] offset:1024
	global_load_dword v19, v15, s[32:33] offset:1536
	global_load_dword v20, v15, s[32:33] offset:2048
	global_load_dword v21, v15, s[32:33] offset:2560
	global_load_dword v22, v15, s[32:33] offset:3072
	global_load_dword v23, v15, s[32:33] offset:3584
	s_waitcnt vmcnt(18)
	v_mul_f32_e32 v84, v48, v32
	v_mul_f32_e32 v85, v48, v33
	v_mul_f32_e32 v86, v48, v34
	v_mul_f32_e32 v87, v48, v35
	v_fmac_f32_e32 v84, v49, v36
	v_fmac_f32_e32 v85, v49, v37
	v_fmac_f32_e32 v86, v49, v38
	v_fmac_f32_e32 v87, v49, v39
	v_fmac_f32_e32 v84, v50, v40
	v_fmac_f32_e32 v85, v50, v41
	v_fmac_f32_e32 v86, v50, v42
	v_fmac_f32_e32 v87, v50, v43
	v_fmac_f32_e32 v84, v51, v44
	v_fmac_f32_e32 v85, v51, v45
	v_fmac_f32_e32 v86, v51, v46
	v_fmac_f32_e32 v87, v51, v47
	ds_write_b128 v30, v[84:87]
	v_lshlrev_b32_e32 v31, 2, v3
	s_waitcnt lgkmcnt(0)
	s_barrier
	ds_read_b32 v88, v31 offset:0
	ds_read_b32 v89, v31 offset:128
	ds_read_b32 v90, v31 offset:256
	ds_read_b32 v91, v31 offset:384
	ds_read_b32 v92, v31 offset:512
	ds_read_b32 v93, v31 offset:640
	ds_read_b32 v94, v31 offset:768
	ds_read_b32 v95, v31 offset:896
	ds_read_b32 v96, v31 offset:1024
	ds_read_b32 v97, v31 offset:1152
	ds_read_b32 v98, v31 offset:1280
	ds_read_b32 v99, v31 offset:1408
	ds_read_b32 v100, v31 offset:1536
	ds_read_b32 v101, v31 offset:1664
	ds_read_b32 v102, v31 offset:1792
	ds_read_b32 v103, v31 offset:1920
	s_waitcnt lgkmcnt(0)
	ds_read_b32 v104, v31 offset:2048
	ds_read_b32 v105, v31 offset:2176
	ds_read_b32 v106, v31 offset:2304
	ds_read_b32 v107, v31 offset:2432
	ds_read_b32 v108, v31 offset:2560
	ds_read_b32 v109, v31 offset:2688
	ds_read_b32 v110, v31 offset:2816
	ds_read_b32 v111, v31 offset:2944
	ds_read_b32 v112, v31 offset:3072
	ds_read_b32 v113, v31 offset:3200
	ds_read_b32 v114, v31 offset:3328
	ds_read_b32 v115, v31 offset:3456
	ds_read_b32 v116, v31 offset:3584
	ds_read_b32 v117, v31 offset:3712
	ds_read_b32 v118, v31 offset:3840
	ds_read_b32 v119, v31 offset:3968
	s_waitcnt lgkmcnt(0)
	v_add_f32_e32 v88, v88, v104
	v_add_f32_e32 v89, v89, v105
	v_add_f32_e32 v90, v90, v106
	v_add_f32_e32 v91, v91, v107
	v_add_f32_e32 v92, v92, v108
	v_add_f32_e32 v93, v93, v109
	v_add_f32_e32 v94, v94, v110
	v_add_f32_e32 v95, v95, v111
	v_add_f32_e32 v96, v96, v112
	v_add_f32_e32 v97, v97, v113
	v_add_f32_e32 v98, v98, v114
	v_add_f32_e32 v99, v99, v115
	v_add_f32_e32 v100, v100, v116
	v_add_f32_e32 v101, v101, v117
	v_add_f32_e32 v102, v102, v118
	v_add_f32_e32 v103, v103, v119
	v_add_f32_e32 v88, v88, v96
	v_add_f32_e32 v89, v89, v97
	v_add_f32_e32 v90, v90, v98
	v_add_f32_e32 v91, v91, v99
	v_add_f32_e32 v92, v92, v100
	v_add_f32_e32 v93, v93, v101
	v_add_f32_e32 v94, v94, v102
	v_add_f32_e32 v95, v95, v103
	v_add_f32_e32 v88, v88, v92
	v_add_f32_e32 v89, v89, v93
	v_add_f32_e32 v90, v90, v94
	v_add_f32_e32 v91, v91, v95
	v_add_f32_e32 v88, v88, v90
	v_add_f32_e32 v89, v89, v91
	v_add_f32_e32 v88, v88, v89
	ds_write_b32 v31, v88 offset:4096
	v_lshlrev_b32_e32 v81, 4, v10
	v_mov_b32_e32 v82, 0
	s_waitcnt lgkmcnt(0)
	s_barrier
	ds_read_b128 v[120:123], v81 offset:4096
	s_waitcnt vmcnt(14)
	s_waitcnt lgkmcnt(0)
	v_mul_f32_e32 v84, v120, v52
	v_mul_f32_e32 v85, v120, v53
	v_mul_f32_e32 v86, v120, v54
	v_mul_f32_e32 v87, v120, v55
	v_fmac_f32_e32 v84, v121, v56
	v_fmac_f32_e32 v85, v121, v57
	v_fmac_f32_e32 v86, v121, v58
	v_fmac_f32_e32 v87, v121, v59
	v_fmac_f32_e32 v84, v122, v60
	v_fmac_f32_e32 v85, v122, v61
	v_fmac_f32_e32 v86, v122, v62
	v_fmac_f32_e32 v87, v122, v63
	v_fmac_f32_e32 v84, v123, v64
	v_fmac_f32_e32 v85, v123, v65
	v_fmac_f32_e32 v86, v123, v66
	v_fmac_f32_e32 v87, v123, v67
	ds_write_b128 v30, v[84:87] offset:8192
	ds_read_b128 v[96:99], v82 offset:4096
	ds_read_b128 v[100:103], v82 offset:4112
	ds_read_b128 v[104:107], v82 offset:4128
	ds_read_b128 v[108:111], v82 offset:4144
	ds_read_b128 v[112:115], v82 offset:4160
	ds_read_b128 v[116:119], v82 offset:4176
	ds_read_b128 v[120:123], v82 offset:4192
	ds_read_b128 v[124:127], v82 offset:4208
	s_waitcnt vmcnt(11)
	v_mul_f32_e32 v92, v76, v68
	v_mul_f32_e32 v93, v76, v69
	v_mul_f32_e32 v94, v76, v70
	v_mul_f32_e32 v95, v76, v71
	v_fmac_f32_e32 v92, v77, v72
	v_fmac_f32_e32 v93, v77, v73
	v_fmac_f32_e32 v94, v77, v74
	v_fmac_f32_e32 v95, v77, v75
	ds_write_b128 v30, v[92:95] offset:12288
	s_waitcnt lgkmcnt(1)
	v_add_f32_e32 v96, v96, v112
	v_add_f32_e32 v97, v97, v113
	v_add_f32_e32 v98, v98, v114
	v_add_f32_e32 v99, v99, v115
	v_add_f32_e32 v100, v100, v116
	v_add_f32_e32 v101, v101, v117
	v_add_f32_e32 v102, v102, v118
	v_add_f32_e32 v103, v103, v119
	v_add_f32_e32 v104, v104, v120
	v_add_f32_e32 v105, v105, v121
	v_add_f32_e32 v106, v106, v122
	v_add_f32_e32 v107, v107, v123
	v_add_f32_e32 v108, v108, v124
	v_add_f32_e32 v109, v109, v125
	v_add_f32_e32 v110, v110, v126
	v_add_f32_e32 v111, v111, v127
	v_add_f32_e32 v96, v96, v104
	v_add_f32_e32 v97, v97, v105
	v_add_f32_e32 v98, v98, v106
	v_add_f32_e32 v99, v99, v107
	v_add_f32_e32 v100, v100, v108
	v_add_f32_e32 v101, v101, v109
	v_add_f32_e32 v102, v102, v110
	v_add_f32_e32 v103, v103, v111
	v_add_f32_e32 v96, v96, v100
	v_add_f32_e32 v97, v97, v101
	v_add_f32_e32 v98, v98, v102
	v_add_f32_e32 v99, v99, v103
	v_add_f32_e32 v96, v96, v98
	v_add_f32_e32 v97, v97, v99
	v_add_f32_e32 v96, v96, v97
	v_mov_b32_e32 v112, v96
	s_waitcnt vmcnt(0)
	v_cvt_pk_bf16_f32 v24, v16, v17
	v_cvt_pk_bf16_f32 v25, v18, v19
	v_cvt_pk_bf16_f32 v26, v20, v21
	v_cvt_pk_bf16_f32 v27, v22, v23
	global_store_dwordx4 v30, v[24:27], s[26:27]
	s_waitcnt lgkmcnt(0)
	s_barrier
	v_cmp_gt_u32_e32 vcc, 0x80, v0
	s_and_saveexec_b64 s[46:47], vcc
	s_cbranch_execz .Lpre_C_done
	v_lshlrev_b32_e32 v83, 2, v0
	ds_read_b32 v96, v83 offset:8192
	ds_read_b32 v97, v83 offset:8704
	ds_read_b32 v98, v83 offset:9216
	ds_read_b32 v99, v83 offset:9728
	ds_read_b32 v100, v83 offset:10240
	ds_read_b32 v101, v83 offset:10752
	ds_read_b32 v102, v83 offset:11264
	ds_read_b32 v103, v83 offset:11776
	ds_read_b32 v104, v83 offset:12288
	ds_read_b32 v105, v83 offset:12800
	ds_read_b32 v106, v83 offset:13312
	ds_read_b32 v107, v83 offset:13824
	ds_read_b32 v108, v83 offset:14336
	ds_read_b32 v109, v83 offset:14848
	ds_read_b32 v110, v83 offset:15360
	ds_read_b32 v111, v83 offset:15872
	s_waitcnt lgkmcnt(0)
	v_add_f32_e32 v96, v96, v100
	v_add_f32_e32 v97, v97, v101
	v_add_f32_e32 v98, v98, v102
	v_add_f32_e32 v99, v99, v103
	v_add_f32_e32 v96, v96, v98
	v_add_f32_e32 v97, v97, v99
	v_add_f32_e32 v96, v96, v97
	v_add_f32_e32 v104, v104, v108
	v_add_f32_e32 v105, v105, v109
	v_add_f32_e32 v106, v106, v110
	v_add_f32_e32 v107, v107, v111
	v_add_f32_e32 v104, v104, v106
	v_add_f32_e32 v105, v105, v107
	v_add_f32_e32 v104, v104, v105
	s_add_u32 s48, s30, 0x40000
	s_addc_u32 s49, s31, 0
	s_lshl_b32 s45, s3, 10
	s_add_u32 s48, s48, s45
	s_addc_u32 s49, s49, 0
	s_cmp_lg_u32 s3, 0
	s_cbranch_scc1 .Lpre_C_nz
	v_add_f32_e32 v96, v96, v78
	v_add_f32_e32 v104, v104, v79
	global_store_dword v83, v80, s[28:29] offset:1024
